# speedup vs baseline: 1.0552x; 1.0552x over previous
.LBB4_11:
	v_lshl_add_u64 v[66:67], s[8:9], 0, v[128:129]
	v_add_co_u32_e32 v66, vcc, s13, v66
	v_lshl_add_u64 v[64:65], s[0:1], 0, v[128:129]
	s_nop 0
	v_addc_co_u32_e32 v67, vcc, 0, v67, vcc
	v_add_co_u32_e32 v64, vcc, s13, v64
	s_and_b32 s14, s15, 1
	s_nop 0
	v_addc_co_u32_e32 v65, vcc, 0, v65, vcc
	global_load_dwordx4 v[112:115], v[66:67], off offset:-4096
	global_load_dwordx4 v[116:119], v[66:67], off
	global_load_dwordx4 v[120:123], v[64:65], off offset:-4096
	global_load_dwordx4 v[124:127], v[64:65], off
	s_add_i32 s15, s15, 1
	s_mul_i32 s18, s14, 0x2400
	v_add_u32_e32 v202, s18, v167
	ds_read_b128 v[204:207], v202
	ds_read_b128 v[208:211], v202 offset:32
	ds_read_b128 v[212:215], v202 offset:64
	ds_read_b128 v[216:219], v202 offset:96
	ds_read_b128 v[220:223], v202 offset:4608
	ds_read_b128 v[224:227], v202 offset:4640
	ds_read_b128 v[228:231], v202 offset:4672
	ds_read_b128 v[232:235], v202 offset:4704
	s_mul_i32 s18, s14, 0x3000
	v_or_b32_e32 v198, s18, v185
	s_waitcnt lgkmcnt(7)
	v_mfma_f32_32x32x16_f16 v[64:79], v[108:111], v[204:207], v[48:63]
	s_waitcnt lgkmcnt(6)
	v_mfma_f32_32x32x16_f16 v[64:79], v[104:107], v[208:211], v[64:79]
	s_waitcnt lgkmcnt(5)
	v_mfma_f32_32x32x16_f16 v[64:79], v[100:103], v[212:215], v[64:79]
	s_waitcnt lgkmcnt(4)
	v_mfma_f32_32x32x16_f16 v[64:79], v[96:99], v[216:219], v[64:79]
	s_waitcnt lgkmcnt(3)
	v_mfma_f32_32x32x16_f16 v[80:95], v[108:111], v[220:223], v[48:63]
	s_waitcnt lgkmcnt(2)
	v_mfma_f32_32x32x16_f16 v[80:95], v[104:107], v[224:227], v[80:95]
	s_setprio 2
	s_nop 7
	v_exp_f32_e32 v64, v64
	v_lshl_add_u64 v[194:195], v[132:133], 0, s[10:11]
	v_mul_f32_e32 v190, v64, v183
	global_store_dword v[194:195], v190, off offset:-128
	v_exp_f32_e32 v65, v65
	v_lshl_add_u64 v[196:197], v[136:137], 0, s[10:11]
	v_mul_f32_e32 v191, v65, v182
	global_store_dword v[196:197], v191, off offset:-128
	v_exp_f32_e32 v66, v66
	v_lshl_add_u64 v[194:195], v[140:141], 0, s[10:11]
	v_mul_f32_e32 v192, v66, v181
	global_store_dword v[194:195], v192, off offset:-128
	v_exp_f32_e32 v67, v67
	v_lshl_add_u64 v[196:197], v[144:145], 0, s[10:11]
	v_mul_f32_e32 v193, v67, v180
	global_store_dword v[196:197], v193, off offset:-128
	v_exp_f32_e32 v68, v68
	v_lshl_add_u64 v[194:195], v[148:149], 0, s[10:11]
	v_mul_f32_e32 v190, v68, v179
	global_store_dword v[194:195], v190, off offset:-128
	v_exp_f32_e32 v69, v69
	v_lshl_add_u64 v[196:197], v[152:153], 0, s[10:11]
	v_mul_f32_e32 v191, v69, v178
	global_store_dword v[196:197], v191, off offset:-128
	v_exp_f32_e32 v70, v70
	v_lshl_add_u64 v[194:195], v[156:157], 0, s[10:11]
	v_mul_f32_e32 v192, v70, v177
	global_store_dword v[194:195], v192, off offset:-128
	v_exp_f32_e32 v71, v71
	v_lshl_add_u64 v[196:197], v[160:161], 0, s[10:11]
	v_mul_f32_e32 v193, v71, v176
	global_store_dword v[196:197], v193, off offset:-128
	s_waitcnt lgkmcnt(1)
	v_mfma_f32_32x32x16_f16 v[80:95], v[100:103], v[228:231], v[80:95]
	v_exp_f32_e32 v72, v72
	v_lshl_add_u64 v[194:195], v[162:163], 0, s[10:11]
	v_mul_f32_e32 v190, v72, v175
	global_store_dword v[194:195], v190, off
	v_exp_f32_e32 v73, v73
	v_lshl_add_u64 v[196:197], v[158:159], 0, s[10:11]
	v_mul_f32_e32 v191, v73, v174
	global_store_dword v[196:197], v191, off
	v_exp_f32_e32 v74, v74
	v_lshl_add_u64 v[194:195], v[154:155], 0, s[10:11]
	v_mul_f32_e32 v192, v74, v173
	global_store_dword v[194:195], v192, off
	v_exp_f32_e32 v75, v75
	v_lshl_add_u64 v[196:197], v[150:151], 0, s[10:11]
	v_mul_f32_e32 v193, v75, v172
	global_store_dword v[196:197], v193, off
	v_exp_f32_e32 v76, v76
	v_lshl_add_u64 v[194:195], v[146:147], 0, s[10:11]
	v_mul_f32_e32 v190, v76, v171
	global_store_dword v[194:195], v190, off
	v_exp_f32_e32 v77, v77
	v_lshl_add_u64 v[196:197], v[142:143], 0, s[10:11]
	v_mul_f32_e32 v191, v77, v170
	global_store_dword v[196:197], v191, off
	v_exp_f32_e32 v78, v78
	v_lshl_add_u64 v[194:195], v[138:139], 0, s[10:11]
	v_mul_f32_e32 v192, v78, v169
	global_store_dword v[194:195], v192, off
	v_exp_f32_e32 v79, v79
	v_lshl_add_u64 v[196:197], v[134:135], 0, s[10:11]
	v_mul_f32_e32 v193, v79, v168
	global_store_dword v[196:197], v193, off
	s_waitcnt lgkmcnt(0)
	v_mfma_f32_32x32x16_f16 v[80:95], v[96:99], v[232:235], v[80:95]
	v_cvt_pk_f16_f32 v236, v64, v65
	v_cvt_pk_f16_f32 v237, v66, v67
	v_cvt_pk_f16_f32 v238, v68, v69
	v_cvt_pk_f16_f32 v239, v70, v71
	v_cvt_pk_f16_f32 v240, v72, v73
	v_cvt_pk_f16_f32 v241, v74, v75
	v_cvt_pk_f16_f32 v242, v76, v77
	v_cvt_pk_f16_f32 v243, v78, v79
	ds_write2_b64 v187, v[236:237], v[238:239] offset1:2
	ds_write2_b64 v187, v[240:241], v[242:243] offset0:4 offset1:6
	ds_read_b64_tr_b16 v[204:205], v186
	ds_read_b64_tr_b16 v[206:207], v186 offset:288
	ds_read_b64_tr_b16 v[208:209], v198
	ds_read_b64_tr_b16 v[210:211], v198 offset:768
	ds_read_b64_tr_b16 v[212:213], v198 offset:64
	ds_read_b64_tr_b16 v[214:215], v198 offset:832
	ds_read_b64_tr_b16 v[216:217], v186 offset:1152
	ds_read_b64_tr_b16 v[218:219], v186 offset:1440
	ds_read_b64_tr_b16 v[220:221], v198 offset:3072
	ds_read_b64_tr_b16 v[222:223], v198 offset:3840
	ds_read_b64_tr_b16 v[224:225], v198 offset:3136
	ds_read_b64_tr_b16 v[226:227], v198 offset:3904
	v_exp_f32_e32 v80, v80
	v_lshl_add_u64 v[194:195], v[132:133], 0, s[10:11]
	v_mul_f32_e32 v190, v80, v183
	global_store_dword v[194:195], v190, off
	v_exp_f32_e32 v81, v81
	v_lshl_add_u64 v[196:197], v[136:137], 0, s[10:11]
	v_mul_f32_e32 v191, v81, v182
	global_store_dword v[196:197], v191, off
	v_exp_f32_e32 v82, v82
	v_lshl_add_u64 v[194:195], v[140:141], 0, s[10:11]
	v_mul_f32_e32 v192, v82, v181
	global_store_dword v[194:195], v192, off
	v_exp_f32_e32 v83, v83
	v_lshl_add_u64 v[196:197], v[144:145], 0, s[10:11]
	v_mul_f32_e32 v193, v83, v180
	global_store_dword v[196:197], v193, off
	v_exp_f32_e32 v84, v84
	v_lshl_add_u64 v[194:195], v[148:149], 0, s[10:11]
	v_mul_f32_e32 v190, v84, v179
	global_store_dword v[194:195], v190, off
	v_exp_f32_e32 v85, v85
	v_lshl_add_u64 v[196:197], v[152:153], 0, s[10:11]
	v_mul_f32_e32 v191, v85, v178
	global_store_dword v[196:197], v191, off
	v_exp_f32_e32 v86, v86
	v_lshl_add_u64 v[194:195], v[156:157], 0, s[10:11]
	v_mul_f32_e32 v192, v86, v177
	global_store_dword v[194:195], v192, off
	v_exp_f32_e32 v87, v87
	v_lshl_add_u64 v[196:197], v[160:161], 0, s[10:11]
	v_mul_f32_e32 v193, v87, v176
	global_store_dword v[196:197], v193, off
	s_waitcnt lgkmcnt(6)
	v_mfma_f32_32x32x16_f16 v[0:15], v[204:207], v[208:211], v[0:15]
	v_mfma_f32_32x32x16_f16 v[16:31], v[204:207], v[212:215], v[16:31]
	v_exp_f32_e32 v88, v88
	v_lshl_add_u64 v[194:195], v[162:163], 0, s[10:11]
	v_mul_f32_e32 v190, v88, v175
	global_store_dword v[194:195], v190, off offset:128
	v_exp_f32_e32 v89, v89
	v_lshl_add_u64 v[196:197], v[158:159], 0, s[10:11]
	v_mul_f32_e32 v191, v89, v174
	global_store_dword v[196:197], v191, off offset:128
	v_exp_f32_e32 v90, v90
	v_lshl_add_u64 v[194:195], v[154:155], 0, s[10:11]
	v_mul_f32_e32 v192, v90, v173
	global_store_dword v[194:195], v192, off offset:128
	v_exp_f32_e32 v91, v91
	v_lshl_add_u64 v[196:197], v[150:151], 0, s[10:11]
	v_mul_f32_e32 v193, v91, v172
	global_store_dword v[196:197], v193, off offset:128
	v_exp_f32_e32 v92, v92
	v_lshl_add_u64 v[194:195], v[146:147], 0, s[10:11]
	v_mul_f32_e32 v190, v92, v171
	global_store_dword v[194:195], v190, off offset:128
	v_exp_f32_e32 v93, v93
	v_lshl_add_u64 v[196:197], v[142:143], 0, s[10:11]
	v_mul_f32_e32 v191, v93, v170
	global_store_dword v[196:197], v191, off offset:128
	v_exp_f32_e32 v94, v94
	v_lshl_add_u64 v[194:195], v[138:139], 0, s[10:11]
	v_mul_f32_e32 v192, v94, v169
	global_store_dword v[194:195], v192, off offset:128
	v_exp_f32_e32 v95, v95
	v_lshl_add_u64 v[196:197], v[134:135], 0, s[10:11]
	v_mul_f32_e32 v193, v95, v168
	global_store_dword v[196:197], v193, off offset:128
	s_waitcnt lgkmcnt(0)
	v_mfma_f32_32x32x16_f16 v[0:15], v[216:219], v[220:223], v[0:15]
	v_mfma_f32_32x32x16_f16 v[16:31], v[216:219], v[224:227], v[16:31]
	v_cvt_pk_f16_f32 v244, v80, v81
	v_cvt_pk_f16_f32 v245, v82, v83
	v_cvt_pk_f16_f32 v246, v84, v85
	v_cvt_pk_f16_f32 v247, v86, v87
	v_cvt_pk_f16_f32 v248, v88, v89
	v_cvt_pk_f16_f32 v249, v90, v91
	v_cvt_pk_f16_f32 v250, v92, v93
	v_cvt_pk_f16_f32 v251, v94, v95
	ds_write2_b64 v131, v[244:245], v[246:247] offset0:32 offset1:34
	ds_write2_b64 v131, v[248:249], v[250:251] offset0:36 offset1:38
	s_setprio 0
	ds_read_b64_tr_b16 v[204:205], v186 offset:2304
	ds_read_b64_tr_b16 v[206:207], v186 offset:2592
	ds_read_b64_tr_b16 v[208:209], v198 offset:6144
	ds_read_b64_tr_b16 v[210:211], v198 offset:6912
	ds_read_b64_tr_b16 v[212:213], v198 offset:6208
	ds_read_b64_tr_b16 v[214:215], v198 offset:6976
	ds_read_b64_tr_b16 v[216:217], v186 offset:3456
	ds_read_b64_tr_b16 v[218:219], v186 offset:3744
	ds_read_b64_tr_b16 v[220:221], v198 offset:9216
	ds_read_b64_tr_b16 v[222:223], v198 offset:9984
	ds_read_b64_tr_b16 v[224:225], v198 offset:9280
	ds_read_b64_tr_b16 v[226:227], v198 offset:10048
	s_waitcnt lgkmcnt(6)
	v_mfma_f32_32x32x16_f16 v[0:15], v[204:207], v[208:211], v[0:15]
	v_mfma_f32_32x32x16_f16 v[16:31], v[204:207], v[212:215], v[16:31]
	s_waitcnt lgkmcnt(0)
	v_mfma_f32_32x32x16_f16 v[0:15], v[216:219], v[220:223], v[0:15]
	v_mfma_f32_32x32x16_f16 v[16:31], v[216:219], v[224:227], v[16:31]
	s_xor_b32 s14, s14, 1
	s_mul_i32 s18, s14, 0x3000
	s_mulk_i32 s14, 0x2400
	s_addk_i32 s14, 0x6000
	s_add_u32 s10, s10, 0x100
	s_addc_u32 s11, s11, 0
	s_add_u32 s8, s8, 0x2000
	s_addc_u32 s9, s9, 0
	s_add_u32 s0, s0, 0x2000
	s_addc_u32 s1, s1, 0
	v_lshl_add_u32 v67, v166, 1, s14
	s_cmpk_eq_i32 s10, 0x1f00
	v_lshl_add_u32 v64, v189, 1, s18
	v_lshl_add_u32 v65, v188, 1, s18
	v_lshl_add_u32 v66, v165, 1, s14
	s_waitcnt vmcnt(35)
	ds_write_b128 v67, v[112:115]
	s_waitcnt vmcnt(34)
	ds_write_b128 v66, v[116:119]
	s_waitcnt vmcnt(33)
	ds_write_b128 v65, v[120:123]
	s_waitcnt vmcnt(32)
	ds_write_b128 v64, v[124:127]
	s_waitcnt lgkmcnt(0)
	s_barrier
	s_cbranch_scc0 .LBB4_11
	s_lshl_b64 s[0:1], s[16:17], 13
	s_add_u32 s0, s4, s0
	s_addc_u32 s1, s5, s1
	v_xor_b32_e32 v52, 0x80000000, v34
	v_xor_b32_e32 v51, 0x80000000, v35
	v_xor_b32_e32 v50, 0x80000000, v32
	v_xor_b32_e32 v49, 0x80000000, v33
	ds_read_b128 v[32:35], v167 offset:9216
	v_xor_b32_e32 v59, 0x80000000, v43
	v_xor_b32_e32 v58, 0x80000000, v40
	v_xor_b32_e32 v57, 0x80000000, v41
	v_xor_b32_e32 v56, 0x80000000, v38
	v_xor_b32_e32 v55, 0x80000000, v39
	v_xor_b32_e32 v54, 0x80000000, v36
	v_xor_b32_e32 v53, 0x80000000, v37
	v_xor_b32_e32 v48, 0x80000000, v46
	v_xor_b32_e32 v47, 0x80000000, v47
	v_xor_b32_e32 v46, 0x80000000, v42
	v_xor_b32_e32 v45, 0x80000000, v45
	v_xor_b32_e32 v44, 0x80000000, v44
	ds_read_b128 v[36:39], v167 offset:9248
	s_add_u32 s0, s0, 0x1f00
	s_waitcnt lgkmcnt(1)
	v_mfma_f32_32x32x16_f16 v[60:75], v[108:111], v[32:35], v[44:59]
	ds_read_b128 v[32:35], v167 offset:13824
	ds_read_b128 v[40:43], v167 offset:13856
	s_addc_u32 s1, s1, 0
	s_waitcnt lgkmcnt(1)
	v_mfma_f32_32x32x16_f16 v[44:59], v[108:111], v[32:35], v[44:59]
	v_mfma_f32_32x32x16_f16 v[60:75], v[104:107], v[36:39], v[60:75]
	ds_read_b128 v[32:35], v167 offset:9280
	ds_read_b128 v[36:39], v167 offset:9312
	s_waitcnt lgkmcnt(2)
	v_mfma_f32_32x32x16_f16 v[44:59], v[104:107], v[40:43], v[44:59]
	s_waitcnt lgkmcnt(1)
	v_mfma_f32_32x32x16_f16 v[60:75], v[100:103], v[32:35], v[60:75]
	ds_read_b128 v[32:35], v167 offset:13888
	ds_read_b128 v[40:43], v167 offset:13920
	s_waitcnt lgkmcnt(1)
	v_mfma_f32_32x32x16_f16 v[44:59], v[100:103], v[32:35], v[44:59]
	v_mfma_f32_32x32x16_f16 v[60:75], v[96:99], v[36:39], v[60:75]
	s_waitcnt lgkmcnt(0)
	v_mfma_f32_32x32x16_f16 v[44:59], v[96:99], v[40:43], v[44:59]
	s_setprio 2
	s_nop 8
	v_exp_f32_e32 v32, v60
	s_nop 0
	v_exp_f32_e32 v34, v44
	v_exp_f32_e32 v35, v61
	v_or_b32_e32 v37, 0x2000, v130
	v_mul_f32_e32 v33, v32, v183
	v_mul_f32_e32 v36, v34, v183
	global_store_dword v130, v33, s[0:1]
	global_store_dword v130, v36, s[0:1] offset:128
	v_exp_f32_e32 v36, v45
	v_mul_f32_e32 v33, v35, v182
	global_store_dword v37, v33, s[0:1]
	v_exp_f32_e32 v33, v62
	v_mul_f32_e32 v38, v36, v182
	global_store_dword v37, v38, s[0:1] offset:128
	v_exp_f32_e32 v37, v46
	v_mul_f32_e32 v38, v33, v181
	v_or_b32_e32 v39, 0x4000, v130
	global_store_dword v39, v38, s[0:1]
	v_exp_f32_e32 v38, v63
	v_mul_f32_e32 v40, v37, v181
	global_store_dword v39, v40, s[0:1] offset:128
	v_exp_f32_e32 v39, v47
	v_mul_f32_e32 v40, v38, v180
	v_cvt_pk_f16_f32 v33, v33, v38
	v_exp_f32_e32 v38, v64
	v_or_b32_e32 v41, 0x6000, v130
	global_store_dword v41, v40, s[0:1]
	v_mul_f32_e32 v40, v39, v180
	global_store_dword v41, v40, s[0:1] offset:128
	v_cvt_pk_f16_f32 v32, v32, v35
	v_cvt_pk_f16_f32 v35, v37, v39
	v_cvt_pk_f16_f32 v34, v34, v36
	v_exp_f32_e32 v40, v48
	v_mul_f32_e32 v36, v38, v179
	v_or_b32_e32 v37, 0x10000, v130
	global_store_dword v37, v36, s[0:1]
	v_exp_f32_e32 v36, v65
	v_exp_f32_e32 v41, v49
	v_mul_f32_e32 v39, v40, v179
	global_store_dword v37, v39, s[0:1] offset:128
	v_mul_f32_e32 v37, v36, v178
	v_or_b32_e32 v39, 0x12000, v130
	global_store_dword v39, v37, s[0:1]
	v_exp_f32_e32 v37, v66
	v_mul_f32_e32 v42, v41, v178
	global_store_dword v39, v42, s[0:1] offset:128
	v_exp_f32_e32 v39, v50
	v_mul_f32_e32 v42, v37, v177
	v_or_b32_e32 v43, 0x14000, v130
	global_store_dword v43, v42, s[0:1]
	v_exp_f32_e32 v42, v67
	v_mul_f32_e32 v44, v39, v177
	global_store_dword v43, v44, s[0:1] offset:128
	v_exp_f32_e32 v43, v51
	v_cvt_pk_f16_f32 v37, v37, v42
	v_cvt_pk_f16_f32 v36, v38, v36
	v_cvt_pk_f16_f32 v38, v40, v41
	v_cvt_pk_f16_f32 v39, v39, v43
	ds_write2_b64 v187, v[32:33], v[36:37] offset1:2
	v_exp_f32_e32 v32, v68
	v_add_u32_e32 v40, 0x800, v187
	ds_write2_b64 v40, v[34:35], v[38:39] offset0:32 offset1:34
	v_exp_f32_e32 v34, v52
	v_exp_f32_e32 v36, v69
	v_exp_f32_e32 v37, v53
	v_mul_f32_e32 v33, v32, v175
	v_or_b32_e32 v35, 0x20000, v130
	global_store_dword v35, v33, s[0:1]
	v_mul_f32_e32 v33, v34, v175
	global_store_dword v35, v33, s[0:1] offset:128
	v_mul_f32_e32 v33, v36, v174
	v_or_b32_e32 v35, 0x22000, v130
	global_store_dword v35, v33, s[0:1]
	v_exp_f32_e32 v33, v70
	v_mul_f32_e32 v38, v37, v174
	global_store_dword v35, v38, s[0:1] offset:128
	v_exp_f32_e32 v35, v54
	v_mul_f32_e32 v38, v33, v173
	v_or_b32_e32 v39, 0x24000, v130
	global_store_dword v39, v38, s[0:1]
	v_exp_f32_e32 v38, v71
	v_mul_f32_e32 v41, v35, v173
	global_store_dword v39, v41, s[0:1] offset:128
	v_exp_f32_e32 v39, v55
	v_mul_f32_e32 v44, v42, v176
	v_mul_f32_e32 v41, v38, v172
	v_or_b32_e32 v42, 0x26000, v130
	v_cvt_pk_f16_f32 v32, v32, v36
	v_exp_f32_e32 v36, v72
	global_store_dword v42, v41, s[0:1]
	v_mul_f32_e32 v41, v39, v172
	v_cvt_pk_f16_f32 v33, v33, v38
	v_exp_f32_e32 v38, v56
	global_store_dword v42, v41, s[0:1] offset:128
	v_exp_f32_e32 v41, v73
	v_exp_f32_e32 v42, v57
	v_cvt_pk_f16_f32 v35, v35, v39
	v_cvt_pk_f16_f32 v34, v34, v37
	v_mul_f32_e32 v37, v36, v171
	v_or_b32_e32 v39, 0x30000, v130
	global_store_dword v39, v37, s[0:1]
	v_mul_f32_e32 v37, v38, v171
	v_or_b32_e32 v45, 0x16000, v130
	global_store_dword v39, v37, s[0:1] offset:128
	v_mul_f32_e32 v37, v41, v170
	v_or_b32_e32 v39, 0x32000, v130
	global_store_dword v45, v44, s[0:1]
	v_mul_f32_e32 v44, v43, v176
	global_store_dword v39, v37, s[0:1]
	v_exp_f32_e32 v37, v74
	v_mul_f32_e32 v43, v42, v170
	global_store_dword v39, v43, s[0:1] offset:128
	v_exp_f32_e32 v39, v58
	global_store_dword v45, v44, s[0:1] offset:128
	v_mul_f32_e32 v43, v37, v169
	v_or_b32_e32 v44, 0x34000, v130
	global_store_dword v44, v43, s[0:1]
	v_exp_f32_e32 v43, v75
	v_mul_f32_e32 v45, v39, v169
	global_store_dword v44, v45, s[0:1] offset:128
	v_exp_f32_e32 v44, v59
	v_mul_f32_e32 v45, v43, v168
	v_or_b32_e32 v46, 0x36000, v130
	global_store_dword v46, v45, s[0:1]
	v_mul_f32_e32 v45, v44, v168
	v_cvt_pk_f16_f32 v37, v37, v43
	v_cvt_pk_f16_f32 v36, v36, v41
	global_store_dword v46, v45, s[0:1] offset:128
	v_cvt_pk_f16_f32 v39, v39, v44
	v_cvt_pk_f16_f32 v38, v38, v42
	ds_write2_b64 v187, v[32:33], v[36:37] offset0:4 offset1:6
	ds_write2_b64 v40, v[34:35], v[38:39] offset0:36 offset1:38
	s_setprio 0
	ds_read_b64_tr_b16 v[32:33], v186
	ds_read_b64_tr_b16 v[34:35], v186 offset:288
	ds_read_b64_tr_b16 v[36:37], v185 offset:12288
	ds_read_b64_tr_b16 v[38:39], v185 offset:13056
	ds_read_b64_tr_b16 v[42:43], v185 offset:13120
	ds_read_b64_tr_b16 v[40:41], v185 offset:12352
	ds_read_b64_tr_b16 v[44:45], v186 offset:1152
	ds_read_b64_tr_b16 v[46:47], v186 offset:1440
	s_waitcnt lgkmcnt(4)
	v_mfma_f32_32x32x16_f16 v[0:15], v[32:35], v[36:39], v[0:15]
	s_waitcnt lgkmcnt(2)
	v_mfma_f32_32x32x16_f16 v[16:31], v[32:35], v[40:43], v[16:31]
	ds_read_b64_tr_b16 v[32:33], v185 offset:15360
	ds_read_b64_tr_b16 v[34:35], v185 offset:16128
	ds_read_b64_tr_b16 v[38:39], v185 offset:16192
	ds_read_b64_tr_b16 v[36:37], v185 offset:15424
	s_waitcnt lgkmcnt(2)
	v_mfma_f32_32x32x16_f16 v[0:15], v[44:47], v[32:35], v[0:15]
	s_waitcnt lgkmcnt(0)
	v_mfma_f32_32x32x16_f16 v[16:31], v[44:47], v[36:39], v[16:31]
	ds_read_b64_tr_b16 v[32:33], v186 offset:2304
	ds_read_b64_tr_b16 v[34:35], v186 offset:2592
	ds_read_b64_tr_b16 v[36:37], v185 offset:18432
	ds_read_b64_tr_b16 v[38:39], v185 offset:19200
	ds_read_b64_tr_b16 v[42:43], v185 offset:19264
	ds_read_b64_tr_b16 v[40:41], v185 offset:18496
	ds_read_b64_tr_b16 v[44:45], v186 offset:3456
	ds_read_b64_tr_b16 v[46:47], v186 offset:3744
	s_waitcnt lgkmcnt(4)
	v_mfma_f32_32x32x16_f16 v[0:15], v[32:35], v[36:39], v[0:15]
	s_waitcnt lgkmcnt(2)
	v_mfma_f32_32x32x16_f16 v[16:31], v[32:35], v[40:43], v[16:31]
	ds_read_b64_tr_b16 v[32:33], v185 offset:21504
	ds_read_b64_tr_b16 v[34:35], v185 offset:22272
	ds_read_b64_tr_b16 v[38:39], v185 offset:22336
	ds_read_b64_tr_b16 v[36:37], v185 offset:21568
	s_waitcnt lgkmcnt(2)
	v_mfma_f32_32x32x16_f16 v[0:15], v[44:47], v[32:35], v[0:15]
	s_waitcnt lgkmcnt(0)
	v_mfma_f32_32x32x16_f16 v[16:31], v[44:47], v[36:39], v[16:31]
	s_lshl_b32 s0, s2, 3
	s_and_b32 s0, s0, 0x7ffff800
	s_add_i32 s3, s3, s0
	s_lshl_b32 s0, s12, 7
	s_and_b32 s0, s0, 0x780
	s_add_u32 s0, s6, s0
	v_mov_b32_e32 v35, 0
	v_or_b32_e32 v32, s3, v184
	s_addc_u32 s1, s7, 0
	v_lshlrev_b32_e32 v34, 1, v164
	v_mov_b32_e32 v33, v35
	v_lshl_add_u64 v[36:37], s[0:1], 0, v[34:35]
	v_lshlrev_b64 v[38:39], 11, v[32:33]
	v_fma_mixlo_f16 v0, v0, v183, 0
	v_lshl_add_u64 v[38:39], v[36:37], 0, v[38:39]
	s_waitcnt vmcnt(63) expcnt(7) lgkmcnt(15)
	s_barrier
	global_store_short v[38:39], v0, off
	v_fma_mixlo_f16 v0, v16, v183, 0
	v_or_b32_e32 v34, 1, v32
	global_store_short v[38:39], v0, off offset:64
	v_lshlrev_b64 v[38:39], 11, v[34:35]
	v_fma_mixlo_f16 v16, v1, v182, 0
	v_lshl_add_u64 v[0:1], v[36:37], 0, v[38:39]
	global_store_short v[0:1], v16, off
	v_fma_mixlo_f16 v16, v17, v182, 0
	v_or_b32_e32 v34, 2, v32
	global_store_short v[0:1], v16, off offset:64
	v_lshlrev_b64 v[0:1], 11, v[34:35]
	v_fma_mixlo_f16 v2, v2, v181, 0
	v_lshl_add_u64 v[0:1], v[36:37], 0, v[0:1]
	global_store_short v[0:1], v2, off
	v_fma_mixlo_f16 v2, v18, v181, 0
	v_or_b32_e32 v34, 3, v32
	global_store_short v[0:1], v2, off offset:64
	v_lshlrev_b64 v[0:1], 11, v[34:35]
	v_fma_mixlo_f16 v2, v3, v180, 0
	v_lshl_add_u64 v[0:1], v[36:37], 0, v[0:1]
	global_store_short v[0:1], v2, off
	v_fma_mixlo_f16 v2, v19, v180, 0
	v_or_b32_e32 v34, 8, v32
	global_store_short v[0:1], v2, off offset:64
	v_lshlrev_b64 v[0:1], 11, v[34:35]
	v_fma_mixlo_f16 v2, v4, v179, 0
	v_lshl_add_u64 v[0:1], v[36:37], 0, v[0:1]
	global_store_short v[0:1], v2, off
	v_fma_mixlo_f16 v2, v20, v179, 0
	v_or_b32_e32 v34, 9, v32
	global_store_short v[0:1], v2, off offset:64
	v_lshlrev_b64 v[0:1], 11, v[34:35]
	v_fma_mixlo_f16 v2, v5, v178, 0
	v_lshl_add_u64 v[0:1], v[36:37], 0, v[0:1]
	global_store_short v[0:1], v2, off
	v_fma_mixlo_f16 v2, v21, v178, 0
	v_or_b32_e32 v34, 10, v32
	global_store_short v[0:1], v2, off offset:64
	v_lshlrev_b64 v[0:1], 11, v[34:35]
	v_fma_mixlo_f16 v2, v6, v177, 0
	v_lshl_add_u64 v[0:1], v[36:37], 0, v[0:1]
	global_store_short v[0:1], v2, off
	v_fma_mixlo_f16 v2, v22, v177, 0
	v_or_b32_e32 v34, 11, v32
	global_store_short v[0:1], v2, off offset:64
	v_lshlrev_b64 v[0:1], 11, v[34:35]
	v_fma_mixlo_f16 v2, v7, v176, 0
	v_lshl_add_u64 v[0:1], v[36:37], 0, v[0:1]
	global_store_short v[0:1], v2, off
	v_fma_mixlo_f16 v2, v23, v176, 0
	v_or_b32_e32 v34, 16, v32
	global_store_short v[0:1], v2, off offset:64
	v_lshlrev_b64 v[0:1], 11, v[34:35]
	v_fma_mixlo_f16 v2, v8, v175, 0
	v_lshl_add_u64 v[0:1], v[36:37], 0, v[0:1]
	global_store_short v[0:1], v2, off
	v_fma_mixlo_f16 v2, v24, v175, 0
	v_or_b32_e32 v34, 17, v32
	global_store_short v[0:1], v2, off offset:64
	v_lshlrev_b64 v[0:1], 11, v[34:35]
	v_fma_mixlo_f16 v2, v9, v174, 0
	v_lshl_add_u64 v[0:1], v[36:37], 0, v[0:1]
	global_store_short v[0:1], v2, off
	v_fma_mixlo_f16 v2, v25, v174, 0
	v_or_b32_e32 v34, 18, v32
	global_store_short v[0:1], v2, off offset:64
	v_lshlrev_b64 v[0:1], 11, v[34:35]
	v_fma_mixlo_f16 v2, v10, v173, 0
	v_lshl_add_u64 v[0:1], v[36:37], 0, v[0:1]
	global_store_short v[0:1], v2, off
	v_fma_mixlo_f16 v2, v26, v173, 0
	v_or_b32_e32 v34, 19, v32
	global_store_short v[0:1], v2, off offset:64
	v_lshlrev_b64 v[0:1], 11, v[34:35]
	v_fma_mixlo_f16 v2, v11, v172, 0
	v_lshl_add_u64 v[0:1], v[36:37], 0, v[0:1]
	global_store_short v[0:1], v2, off
	v_fma_mixlo_f16 v2, v27, v172, 0
	v_or_b32_e32 v34, 24, v32
	global_store_short v[0:1], v2, off offset:64
	v_lshlrev_b64 v[0:1], 11, v[34:35]
	v_fma_mixlo_f16 v2, v12, v171, 0
	v_lshl_add_u64 v[0:1], v[36:37], 0, v[0:1]
	global_store_short v[0:1], v2, off
	v_fma_mixlo_f16 v2, v28, v171, 0
	v_or_b32_e32 v34, 25, v32
	global_store_short v[0:1], v2, off offset:64
	v_lshlrev_b64 v[0:1], 11, v[34:35]
	v_fma_mixlo_f16 v2, v13, v170, 0
	v_lshl_add_u64 v[0:1], v[36:37], 0, v[0:1]
	global_store_short v[0:1], v2, off
	v_fma_mixlo_f16 v2, v29, v170, 0
	v_or_b32_e32 v34, 26, v32
	global_store_short v[0:1], v2, off offset:64
	v_lshlrev_b64 v[0:1], 11, v[34:35]
	v_fma_mixlo_f16 v2, v14, v169, 0
	v_lshl_add_u64 v[0:1], v[36:37], 0, v[0:1]
	global_store_short v[0:1], v2, off
	v_fma_mixlo_f16 v2, v30, v169, 0
	v_or_b32_e32 v34, 27, v32
	global_store_short v[0:1], v2, off offset:64
	v_lshlrev_b64 v[0:1], 11, v[34:35]
	v_fma_mixlo_f16 v2, v15, v168, 0
	v_lshl_add_u64 v[0:1], v[36:37], 0, v[0:1]
	global_store_short v[0:1], v2, off
	v_fma_mixlo_f16 v2, v31, v168, 0
	global_store_short v[0:1], v2, off offset:64
	s_endpgm
	.p2alignl 8, 3212836864

	.amdhsa_kernel _Z11attn_kernelILi0EEvPKDF16_S1_S1_PKfS3_PfPDF16_
		.amdhsa_group_segment_fixed_size 61440
		.amdhsa_private_segment_fixed_size 0
		.amdhsa_kernarg_size 56
		.amdhsa_user_sgpr_count 2
		.amdhsa_user_sgpr_dispatch_ptr 0
		.amdhsa_user_sgpr_queue_ptr 0
		.amdhsa_user_sgpr_kernarg_segment_ptr 1
		.amdhsa_user_sgpr_dispatch_id 0
		.amdhsa_user_sgpr_kernarg_preload_length 0
		.amdhsa_user_sgpr_kernarg_preload_offset 0
		.amdhsa_user_sgpr_private_segment_size 0
		.amdhsa_uses_dynamic_stack 0
		.amdhsa_enable_private_segment 0
		.amdhsa_system_sgpr_workgroup_id_x 1
		.amdhsa_system_sgpr_workgroup_id_y 0
		.amdhsa_system_sgpr_workgroup_id_z 0
		.amdhsa_system_sgpr_workgroup_info 0
		.amdhsa_system_vgpr_workitem_id 0
		.amdhsa_next_free_vgpr 252
		.amdhsa_next_free_sgpr 96
		.amdhsa_accum_offset 252
		.amdhsa_reserve_vcc 1
		.amdhsa_float_round_mode_32 0
		.amdhsa_float_round_mode_16_64 0
		.amdhsa_float_denorm_mode_32 3
		.amdhsa_float_denorm_mode_16_64 3
		.amdhsa_dx10_clamp 1
		.amdhsa_ieee_mode 1
		.amdhsa_fp16_overflow 0
		.amdhsa_tg_split 0
		.amdhsa_exception_fp_ieee_invalid_op 0
		.amdhsa_exception_fp_denorm_src 0
		.amdhsa_exception_fp_ieee_div_zero 0
		.amdhsa_exception_fp_ieee_overflow 0
		.amdhsa_exception_fp_ieee_underflow 0
		.amdhsa_exception_fp_ieee_inexact 0
		.amdhsa_exception_int_div_zero 0
	.end_amdhsa_kernel

amdhsa.kernels:
  - .agpr_count:     0
    .args:
      - .actual_access:  read_only
        .address_space:  global
        .offset:         0
        .size:           8
        .value_kind:     global_buffer
      - .actual_access:  read_only
        .address_space:  global
        .offset:         8
        .size:           8
        .value_kind:     global_buffer
      - .actual_access:  read_only
        .address_space:  global
        .offset:         16
        .size:           8
        .value_kind:     global_buffer
      - .actual_access:  read_only
        .address_space:  global
        .offset:         24
        .size:           8
        .value_kind:     global_buffer
      - .actual_access:  read_only
        .address_space:  global
        .offset:         32
        .size:           8
        .value_kind:     global_buffer
      - .actual_access:  write_only
        .address_space:  global
        .offset:         40
        .size:           8
        .value_kind:     global_buffer
      - .actual_access:  write_only
        .address_space:  global
        .offset:         48
        .size:           8
        .value_kind:     global_buffer
    .group_segment_fixed_size: 0
    .kernarg_segment_align: 8
    .kernarg_segment_size: 56
    .language:       OpenCL C
    .language_version:
      - 2
      - 0
    .max_flat_workgroup_size: 256
    .name:           _Z10cvt_kernelPKfS0_S0_S0_S0_PDF16_S1_
    .private_segment_fixed_size: 0
    .sgpr_count:     22
    .sgpr_spill_count: 0
    .symbol:         _Z10cvt_kernelPKfS0_S0_S0_S0_PDF16_S1_.kd
    .uniform_work_group_size: 1
    .uses_dynamic_stack: false
    .vgpr_count:     14
    .vgpr_spill_count: 0
    .wavefront_size: 64
  - .agpr_count:     0
    .args:
      - .actual_access:  read_only
        .address_space:  global
        .offset:         0
        .size:           8
        .value_kind:     global_buffer
      - .actual_access:  read_only
        .address_space:  global
        .offset:         8
        .size:           8
        .value_kind:     global_buffer
      - .actual_access:  write_only
        .address_space:  global
        .offset:         16
        .size:           8
        .value_kind:     global_buffer
      - .actual_access:  write_only
        .address_space:  global
        .offset:         24
        .size:           8
        .value_kind:     global_buffer
    .group_segment_fixed_size: 18432
    .kernarg_segment_align: 8
    .kernarg_segment_size: 32
    .language:       OpenCL C
    .language_version:
      - 2
      - 0
    .max_flat_workgroup_size: 256
    .name:           _Z12stats_kernelPKDF16_S0_PfS1_
    .private_segment_fixed_size: 0
    .sgpr_count:     19
    .sgpr_spill_count: 0
    .symbol:         _Z12stats_kernelPKDF16_S0_PfS1_.kd
    .uniform_work_group_size: 1
    .uses_dynamic_stack: false
    .vgpr_count:     100
    .vgpr_spill_count: 0
    .wavefront_size: 64
  - .agpr_count:     0
    .args:
      - .actual_access:  read_only
        .address_space:  global
        .offset:         0
        .size:           8
        .value_kind:     global_buffer
      - .actual_access:  read_only
        .address_space:  global
        .offset:         8
        .size:           8
        .value_kind:     global_buffer
      - .actual_access:  read_only
        .address_space:  global
        .offset:         16
        .size:           8
        .value_kind:     global_buffer
      - .actual_access:  read_only
        .address_space:  global
        .offset:         24
        .size:           8
        .value_kind:     global_buffer
      - .actual_access:  write_only
        .address_space:  global
        .offset:         32
        .size:           8
        .value_kind:     global_buffer
      - .actual_access:  write_only
        .address_space:  global
        .offset:         40
        .size:           8
        .value_kind:     global_buffer
      - .actual_access:  write_only
        .address_space:  global
        .offset:         48
        .size:           8
        .value_kind:     global_buffer
      - .actual_access:  read_only
        .address_space:  global
        .offset:         56
        .size:           8
        .value_kind:     global_buffer
      - .offset:         64
        .size:           4
        .value_kind:     by_value
    .group_segment_fixed_size: 0
    .kernarg_segment_align: 8
    .kernarg_segment_size: 68
    .language:       OpenCL C
    .language_version:
      - 2
      - 0
    .max_flat_workgroup_size: 512
    .name:           _Z11gemm_kernelILi256ELi192ELi4ELi2ELi0EEvPKDF16_S1_PKfS3_PDF16_S4_S4_Pfi
    .private_segment_fixed_size: 0
    .sgpr_count:     27
    .sgpr_spill_count: 0
    .symbol:         _Z11gemm_kernelILi256ELi192ELi4ELi2ELi0EEvPKDF16_S1_PKfS3_PDF16_S4_S4_Pfi.kd
    .uniform_work_group_size: 1
    .uses_dynamic_stack: false
    .vgpr_count:     249
    .vgpr_spill_count: 0
    .wavefront_size: 64
  - .agpr_count:     0
    .args:
      - .actual_access:  read_only
        .address_space:  global
        .offset:         0
        .size:           8
        .value_kind:     global_buffer
      - .actual_access:  read_only
        .address_space:  global
        .offset:         8
        .size:           8
        .value_kind:     global_buffer
      - .actual_access:  read_only
        .address_space:  global
        .offset:         16
        .size:           8
        .value_kind:     global_buffer
      - .actual_access:  read_only
        .address_space:  global
        .offset:         24
        .size:           8
        .value_kind:     global_buffer
      - .actual_access:  read_only
        .address_space:  global
        .offset:         32
        .size:           8
        .value_kind:     global_buffer
      - .actual_access:  read_only
        .address_space:  global
        .offset:         40
        .size:           8
        .value_kind:     global_buffer
      - .actual_access:  read_only
        .address_space:  global
        .offset:         48
        .size:           8
        .value_kind:     global_buffer
      - .actual_access:  write_only
        .address_space:  global
        .offset:         56
        .size:           8
        .value_kind:     global_buffer
      - .offset:         64
        .size:           4
        .value_kind:     by_value
    .group_segment_fixed_size: 0
    .kernarg_segment_align: 8
    .kernarg_segment_size: 68
    .language:       OpenCL C
    .language_version:
      - 2
      - 0
    .max_flat_workgroup_size: 512
    .name:           _Z11gemm_kernelILi128ELi128ELi4ELi2ELi1EEvPKDF16_S1_PKfS3_PDF16_S4_S4_Pfi
    .private_segment_fixed_size: 0
    .sgpr_count:     19
    .sgpr_spill_count: 0
    .symbol:         _Z11gemm_kernelILi128ELi128ELi4ELi2ELi1EEvPKDF16_S1_PKfS3_PDF16_S4_S4_Pfi.kd
    .uniform_work_group_size: 1
    .uses_dynamic_stack: false
    .vgpr_count:     88
    .vgpr_spill_count: 0
    .wavefront_size: 64
  - .agpr_count:     0
    .args:
      - .actual_access:  read_only
        .address_space:  global
        .offset:         0
        .size:           8
        .value_kind:     global_buffer
      - .actual_access:  read_only
        .address_space:  global
        .offset:         8
        .size:           8
        .value_kind:     global_buffer
      - .actual_access:  read_only
        .address_space:  global
        .offset:         16
        .size:           8
        .value_kind:     global_buffer
      - .actual_access:  read_only
        .address_space:  global
        .offset:         24
        .size:           8
        .value_kind:     global_buffer
      - .actual_access:  read_only
        .address_space:  global
        .offset:         32
        .size:           8
        .value_kind:     global_buffer
      - .actual_access:  write_only
        .address_space:  global
        .offset:         40
        .size:           8
        .value_kind:     global_buffer
      - .actual_access:  write_only
        .address_space:  global
        .offset:         48
        .size:           8
        .value_kind:     global_buffer
    .group_segment_fixed_size: 61440
    .kernarg_segment_align: 8
    .kernarg_segment_size: 56
    .language:       OpenCL C
    .language_version:
      - 2
      - 0
    .max_flat_workgroup_size: 256
    .name:           _Z11attn_kernelILi0EEvPKDF16_S1_S1_PKfS3_PfPDF16_
    .private_segment_fixed_size: 0
    .sgpr_count:     30
    .sgpr_spill_count: 0
    .symbol:         _Z11attn_kernelILi0EEvPKDF16_S1_S1_PKfS3_PfPDF16_.kd
    .uniform_work_group_size: 1
    .uses_dynamic_stack: false
    .vgpr_count:     252
    .vgpr_spill_count: 0
    .wavefront_size: 64
